# prologue hyena tasks: bid rotated so that an XCD owns 32 consecutive tasks per round (backward halves of neighbouring tasks share lines)
# speedup vs baseline: 1.0133x; 1.0074x over previous
;     ...
;     const float lo = -4.605170185988091f / 1.5f, hi = -4.605170185988091f / 0.3f;
;     const float delta = fabsf(lo + (float)tid * ((hi - lo) / 511.f));
;     float* HF = isctx ? (float*)(P.ws + WS_HFC) + (size_t)tid * 512 + 256 : (float*)(P.ws + WS_HF) + (size_t)tid * 32768 + LSEQ;
;     ...
;         for (int task = bid; task < 520; task += nb) hyena_filter_task(P, sm, task, rep == 0 ? 1 : 0);
.Ltr_done:
	s_cmpk_gt_i32 s44, 0x207
	s_cbranch_scc1 .LBB0_109
	v_cvt_f32_u32_e32 v2, v0
	v_readlane_b32 s12, v253, 51
	v_mul_u32_u24_e32 v3, 0x208, v0
	v_lshlrev_b32_e32 v6, 2, v202
	v_mov_b32_e32 v7, 0
	v_readlane_b32 s13, v253, 52
	v_readlane_b32 s14, v253, 53
	v_readlane_b32 s15, v253, 54
	v_readlane_b32 s18, v253, 57
	v_readlane_b32 s19, v253, 58
	v_readlane_b32 s0, v252, 19
	v_mov_b32_e32 v67, 0xc0447cbd
	v_lshl_add_u64 v[8:9], s[12:13], 0, v[6:7]
	v_lshl_add_u64 v[10:11], s[14:15], 0, v[6:7]
	v_lshl_add_u64 v[12:13], s[18:19], 0, v[6:7]
	v_lshlrev_b32_e32 v6, 2, v3
	v_readlane_b32 s1, v252, 20
	v_readlane_b32 s2, v252, 21
	v_readlane_b32 s3, v252, 22
	v_fmac_f32_e32 v67, 0xbcc4df2d, v2
	s_mov_b64 s[0:1], 0x40662400
	v_lshl_add_u64 v[2:3], s[2:3], 0, v[6:7]
	v_lshl_add_u64 v[14:15], v[2:3], 0, s[0:1]
	v_mul_u32_u24_e32 v3, 0x84, v1
	v_readlane_b32 s0, v253, 35
	v_add3_u32 v69, v3, 0, 16
	v_mov_b32_e32 v3, 0x200
	v_readlane_b32 s10, v253, 45
	v_readlane_b32 s11, v253, 46
	v_readlane_b32 s16, v253, 55
	v_readlane_b32 s17, v253, 56
	v_readlane_b32 s20, v253, 59
	v_readlane_b32 s21, v253, 60
	v_readlane_b32 s24, v253, 63
	v_readlane_b32 s25, v252, 0
	v_readlane_b32 s26, v252, 1
	v_readlane_b32 s27, v252, 2
	v_lshlrev_b32_e32 v2, 2, v0
	v_lshl_or_b32 v6, v202, 2, v3
	v_readlane_b32 s12, v253, 47
	v_readlane_b32 s13, v253, 48
	v_readlane_b32 s14, v253, 49
	v_readlane_b32 s15, v253, 50
	v_mov_b32_e32 v3, v7
	s_mov_b32 s10, 0x54442d18
	v_add3_u32 v68, v2, 0, 16
	v_lshl_add_u64 v[16:17], s[14:15], 0, v[6:7]
	v_lshl_add_u64 v[18:19], s[16:17], 0, v[6:7]
	v_lshl_add_u64 v[20:21], s[20:21], 0, v[2:3]
	s_mov_b32 s11, 0x401921fb
	v_mov_b32_e32 v23, 0x3f7fff90
	s_brev_b32 s24, 18
	s_mov_b32 s25, 0xfe5163ab
	s_mov_b32 s26, 0x3c439041
	s_mov_b32 s27, 0xdb629599
	s_mov_b32 s28, 0xf534ddc0
	s_mov_b32 s29, 0xfc2757d1
	s_mov_b32 s30, 0x4e441529
	s_mov_b32 s31, 0xa2f9836e
	s_mov_b32 s34, 0x3fc90fda
	s_mov_b32 s35, 0x3f22f983
	s_mov_b32 s36, 0xbfc90fda
	v_mov_b32_e32 v70, 0x3c0881c4
	v_mov_b32_e32 v71, 0xbab64f3b
	s_movk_i32 s37, 0x1f8
	s_mov_b64 s[12:13], 0x400
	s_movk_i32 s38, 0x5ff
	s_add_i32 s39, 0, 0x1090
	s_mov_b32 s40, 0x3fb8aa3b
	s_mov_b32 s41, 0xc2ce8ed0
	s_mov_b32 s42, 0x42b17218
	v_not_b32_e32 v72, 63
	v_not_b32_e32 v73, 31
	v_mov_b32_e32 v74, 0xffc00000
	v_mov_b32_e32 v75, 0x7fc00000
	v_mov_b32_e32 v76, 0x7f800000
	v_readlane_b32 s14, v253, 10
	s_cmpk_lg_u32 s14, 0x100
	s_mov_b32 s14, s44
	s_cbranch_scc1 .Lhy_xcd
	s_and_b32 s14, s44, 7
	s_lshl_b32 s14, s14, 5
	s_lshr_b32 s96, s44, 3
	s_or_b32 s14, s14, s96
;     ...
;     for (int e = tid; e < 32 * 64; e += NTHR) {
;         const int pp = e >> 6, j = e & 63;
;         float s = b1[j];
; #pragma unroll 4
;         for (int i = 0; i < 33; ++i) s += zemb[pp * 33 + i] * w1[i * 64 + j];
;         h1[e] = sinf(fq[j] * s);
;     }
;     __syncthreads();
;     for (int e = tid; e < 32 * 64; e += NTHR) {
;         const int pp = e >> 6, j = e & 63;
;         float s = b2[j];
; #pragma unroll 4
;         for (int i = 0; i < 64; ++i) s += h1[pp * 64 + i] * w2[i * 64 + j];
;         h2[e] = sinf(fq[j] * s);
.Lhy_xcd:
	v_readlane_b32 s22, v253, 61
	v_readlane_b32 s23, v253, 62
	v_readlane_b32 s1, v253, 36
	v_readlane_b32 s2, v253, 37
	v_readlane_b32 s3, v253, 38
	v_readlane_b32 s4, v253, 39
	v_readlane_b32 s5, v253, 40
	v_readlane_b32 s6, v253, 41
	v_readlane_b32 s7, v253, 42
	v_readlane_b32 s8, v253, 43
	v_readlane_b32 s9, v253, 44
	global_load_dword v104, v[16:17], off offset:-512
	global_load_dword v105, v[16:17], off offset:-256
	global_load_dword v106, v[16:17], off
	global_load_dword v107, v[16:17], off offset:256
	global_load_dword v108, v[16:17], off offset:512
	global_load_dword v109, v[16:17], off offset:768
	global_load_dword v110, v[16:17], off offset:1024
	global_load_dword v111, v[16:17], off offset:1280
	global_load_dword v112, v[16:17], off offset:1536
	global_load_dword v113, v[16:17], off offset:1792
	global_load_dword v114, v[16:17], off offset:2048
	global_load_dword v115, v[16:17], off offset:2304
	global_load_dword v116, v[16:17], off offset:2560
	global_load_dword v117, v[16:17], off offset:2816
	global_load_dword v118, v[16:17], off offset:3072
	global_load_dword v119, v[16:17], off offset:3328
	s_mov_b64 s[98:99], 0x1000
	v_lshl_add_u64 v[2:3], v[16:17], 0, s[98:99]
	global_load_dword v120, v[2:3], off offset:-512
	global_load_dword v121, v[2:3], off offset:-256
	global_load_dword v122, v[2:3], off
	global_load_dword v123, v[2:3], off offset:256
	global_load_dword v124, v[2:3], off offset:512
	global_load_dword v125, v[2:3], off offset:768
	global_load_dword v126, v[2:3], off offset:1024
	global_load_dword v127, v[2:3], off offset:1280
	global_load_dword v128, v[2:3], off offset:1536
	global_load_dword v129, v[2:3], off offset:1792
	global_load_dword v130, v[2:3], off offset:2048
	global_load_dword v131, v[2:3], off offset:2304
	global_load_dword v132, v[2:3], off offset:2560
	global_load_dword v133, v[2:3], off offset:2816
	global_load_dword v134, v[2:3], off offset:3072
	global_load_dword v135, v[2:3], off offset:3328
	s_mov_b64 s[98:99], 0x2000
	v_lshl_add_u64 v[2:3], v[16:17], 0, s[98:99]
	global_load_dword v136, v[2:3], off offset:-512
	global_load_dword v137, v[18:19], off offset:-512
	global_load_dword v138, v[18:19], off offset:-256
	global_load_dword v139, v[18:19], off
	global_load_dword v140, v[18:19], off offset:256
	global_load_dword v141, v[18:19], off offset:512
	global_load_dword v142, v[18:19], off offset:768
	global_load_dword v143, v[18:19], off offset:1024
	global_load_dword v144, v[18:19], off offset:1280
	global_load_dword v145, v[18:19], off offset:1536
	global_load_dword v146, v[18:19], off offset:1792
	global_load_dword v147, v[18:19], off offset:2048
	global_load_dword v148, v[18:19], off offset:2304
	global_load_dword v149, v[18:19], off offset:2560
	global_load_dword v150, v[18:19], off offset:2816
	global_load_dword v151, v[18:19], off offset:3072
	global_load_dword v152, v[18:19], off offset:3328
	s_mov_b64 s[98:99], 0x1000
	v_lshl_add_u64 v[2:3], v[18:19], 0, s[98:99]
	global_load_dword v153, v[2:3], off offset:-512
	global_load_dword v154, v[2:3], off offset:-256
	global_load_dword v155, v[2:3], off
	global_load_dword v156, v[2:3], off offset:256
	global_load_dword v157, v[2:3], off offset:512
	global_load_dword v158, v[2:3], off offset:768
	global_load_dword v159, v[2:3], off offset:1024
	global_load_dword v160, v[2:3], off offset:1280
	global_load_dword v161, v[2:3], off offset:1536
	global_load_dword v162, v[2:3], off offset:1792
	global_load_dword v163, v[2:3], off offset:2048
	global_load_dword v164, v[2:3], off offset:2304
	global_load_dword v165, v[2:3], off offset:2560
	global_load_dword v166, v[2:3], off offset:2816
	global_load_dword v167, v[2:3], off offset:3072
	global_load_dword v168, v[2:3], off offset:3328
	s_mov_b64 s[98:99], 0x2000
	v_lshl_add_u64 v[2:3], v[18:19], 0, s[98:99]
	global_load_dword v169, v[2:3], off offset:-512
	global_load_dword v170, v[2:3], off offset:-256
	global_load_dword v171, v[2:3], off
	global_load_dword v172, v[2:3], off offset:256
	global_load_dword v173, v[2:3], off offset:512
	global_load_dword v174, v[2:3], off offset:768
	global_load_dword v175, v[2:3], off offset:1024
	global_load_dword v176, v[2:3], off offset:1280
	global_load_dword v177, v[2:3], off offset:1536
	global_load_dword v178, v[2:3], off offset:1792
	global_load_dword v179, v[2:3], off offset:2048
	global_load_dword v180, v[2:3], off offset:2304
	global_load_dword v181, v[2:3], off offset:2560
	global_load_dword v182, v[2:3], off offset:2816
	global_load_dword v183, v[2:3], off offset:3072
	global_load_dword v184, v[2:3], off offset:3328
	s_mov_b64 s[98:99], 0x3000
	v_lshl_add_u64 v[2:3], v[18:19], 0, s[98:99]
	global_load_dword v185, v[2:3], off offset:-512
	global_load_dword v186, v[2:3], off offset:-256
	global_load_dword v187, v[2:3], off
	global_load_dword v188, v[2:3], off offset:256
	global_load_dword v189, v[2:3], off offset:512
	global_load_dword v190, v[2:3], off offset:768
	global_load_dword v191, v[2:3], off offset:1024
	global_load_dword v192, v[2:3], off offset:1280
	global_load_dword v193, v[2:3], off offset:1536
	global_load_dword v194, v[2:3], off offset:1792
	global_load_dword v195, v[2:3], off offset:2048
	global_load_dword v196, v[2:3], off offset:2304
	global_load_dword v197, v[2:3], off offset:2560
	global_load_dword v198, v[2:3], off offset:2816
	global_load_dword v199, v[2:3], off offset:3072
	global_load_dword v200, v[2:3], off offset:3328
	s_branch .LBB0_37
